# plus non-temporal loads for the V^T chunk image in mlstm_c (last use)
# speedup vs baseline: 1.0004x; 1.0004x over previous
.LBB0_659:
	s_ashr_i32 s70, s39, 6
	s_ashr_i32 s71, s70, 31
	s_and_b32 s74, s33, 0x1f80
	s_lshl_b64 s[30:31], s[70:71], 22
	v_lshl_add_u64 v[50:51], v[162:163], 0, s[30:31]
	s_lshl_b32 s88, s74, 1
	v_lshl_add_u64 v[50:51], v[50:51], 0, s[88:89]
	v_lshl_add_u64 v[94:95], v[50:51], 0, v[160:161]
	global_load_dword v114, v[198:199], off
	global_load_dwordx4 v[50:53], v[94:95], off offset:48 nt
	global_load_dwordx4 v[54:57], v[94:95], off offset:32 nt
	global_load_dwordx4 v[58:61], v[94:95], off offset:16 nt
	global_load_dwordx4 v[62:65], v[94:95], off nt
	global_load_dwordx4 v[66:69], v[200:201], off offset:-16
	global_load_dwordx4 v[70:73], v[200:201], off offset:-32
	global_load_dwordx4 v[74:77], v[200:201], off offset:-48
	global_load_dwordx4 v[78:81], v[200:201], off offset:-64
	global_load_dwordx4 v[82:85], v[94:95], off offset:112 nt
	global_load_dwordx4 v[86:89], v[94:95], off offset:96 nt
	global_load_dwordx4 v[90:93], v[94:95], off offset:80 nt
	s_nop 0
	global_load_dwordx4 v[94:97], v[94:95], off offset:64 nt
	s_nop 0
	global_load_dwordx4 v[98:101], v[200:201], off offset:48
	global_load_dwordx4 v[102:105], v[200:201], off offset:32
	global_load_dwordx4 v[106:109], v[200:201], off offset:16
	global_load_dwordx4 v[110:113], v[200:201], off
	s_mul_hi_i32 s30, s70, 0x2aaaaaab
	s_lshr_b32 s31, s30, 31
	s_add_i32 s72, s30, s31
	s_ashr_i32 s73, s72, 31
	s_lshl_b64 s[30:31], s[72:73], 13
	s_or_b32 s30, s30, s74
	s_mul_i32 s71, s72, 6
	v_lshl_add_u64 v[204:205], s[30:31], 0, v[164:165]
	v_mov_b64_e32 v[252:253], s[92:93]
	s_sub_i32 s88, s70, s71
	v_mad_u64_u32 v[252:253], s[70:71], v204, s3, v[252:253]
	s_lshl_b32 s70, s88, 7
	s_ashr_i32 s71, s70, 31
	v_mad_i32_i24 v253, v205, s3, v253
	s_lshl_b64 s[70:71], s[70:71], 1
	v_lshl_add_u64 v[252:253], v[252:253], 0, s[70:71]
	v_mov_b32_e32 v203, v161
	v_lshl_add_u64 v[244:245], v[252:253], 0, v[202:203]
	global_load_dwordx4 v[232:235], v[244:245], off
	global_load_dwordx4 v[236:239], v[244:245], off offset:64
	global_load_dwordx4 v[240:243], v[244:245], off offset:128
	global_load_dwordx4 v[248:251], v[244:245], off offset:192
	global_load_dword v210, v161, s[22:23]
	s_waitcnt vmcnt(21)
	ds_write_b32 v1, v114
	s_waitcnt vmcnt(17)
	ds_write_b128 v183, v[62:65]
	s_waitcnt vmcnt(13)
	ds_write_b128 v212, v[78:81]
	ds_write_b128 v183, v[58:61] offset:16
	ds_write_b128 v212, v[74:77] offset:16
	ds_write_b128 v183, v[54:57] offset:32
	ds_write_b128 v212, v[70:73] offset:32
	ds_write_b128 v183, v[50:53] offset:48
	ds_write_b128 v212, v[66:69] offset:48
	s_waitcnt vmcnt(9)
	ds_write_b128 v183, v[94:97] offset:64
	s_waitcnt vmcnt(5)
	ds_write_b128 v212, v[110:113] offset:64
	ds_write_b128 v183, v[90:93] offset:80
	ds_write_b128 v212, v[106:109] offset:80
	ds_write_b128 v183, v[86:89] offset:96
	ds_write_b128 v212, v[102:105] offset:96
	ds_write_b128 v183, v[82:85] offset:112
	ds_write_b128 v212, v[98:101] offset:112
	s_waitcnt lgkmcnt(0)
	s_barrier
	ds_read_b32 v130, v159
	ds_read_b32 v208, v171
	ds_read_b128 v[54:57], v173
	ds_read_b128 v[58:61], v173 offset:16
	v_lshl_add_u64 v[138:139], v[166:167], 0, s[70:71]
	v_or_b32_e32 v131, s30, v158
	s_andn2_b64 vcc, exec, s[94:95]
	ds_read_b128 v[74:77], v213 offset:4416
	ds_read_b128 v[78:81], v213 offset:8768
	ds_read_b128 v[82:85], v213 offset:13120
	s_waitcnt vmcnt(0)
	v_mov_b32_e32 v50, v232
	v_mov_b32_e32 v51, v233
	v_mov_b32_e32 v52, v234
	v_mov_b32_e32 v53, v235
	v_and_b32_e32 v65, 0xffff0000, v50
	v_lshlrev_b32_e32 v64, 16, v50
	s_waitcnt lgkmcnt(4)
	v_mul_f32_e32 v55, v55, v65
	v_fmac_f32_e32 v55, v54, v64
	v_lshlrev_b32_e32 v54, 16, v51
	v_fmac_f32_e32 v55, v56, v54
	v_and_b32_e32 v54, 0xffff0000, v51
	v_fmac_f32_e32 v55, v57, v54
	v_lshlrev_b32_e32 v54, 16, v52
	s_waitcnt lgkmcnt(3)
	v_fmac_f32_e32 v55, v58, v54
	v_and_b32_e32 v54, 0xffff0000, v52
	v_fmac_f32_e32 v55, v59, v54
	v_lshlrev_b32_e32 v54, 16, v53
	v_fmac_f32_e32 v55, v60, v54
	v_and_b32_e32 v54, 0xffff0000, v53
	v_fmac_f32_e32 v55, v61, v54
	v_add_f32_e32 v64, 0, v55
	ds_read_b128 v[58:61], v173 offset:128
	v_mov_b32_e32 v54, v236
	v_mov_b32_e32 v55, v237
	v_mov_b32_e32 v56, v238
	v_mov_b32_e32 v57, v239
	v_and_b32_e32 v66, 0xffff0000, v54
	v_lshlrev_b32_e32 v65, 16, v54
	s_waitcnt lgkmcnt(0)
	v_mul_f32_e32 v66, v59, v66
	v_fmac_f32_e32 v66, v58, v65
	v_lshlrev_b32_e32 v58, 16, v55
	v_fmac_f32_e32 v66, v60, v58
	v_and_b32_e32 v58, 0xffff0000, v55
	v_fmac_f32_e32 v66, v61, v58
	ds_read_b128 v[58:61], v173 offset:144
	v_lshlrev_b32_e32 v65, 16, v56
	s_waitcnt lgkmcnt(0)
	v_fmac_f32_e32 v66, v58, v65
	v_and_b32_e32 v58, 0xffff0000, v56
	v_fmac_f32_e32 v66, v59, v58
	v_lshlrev_b32_e32 v58, 16, v57
	v_fmac_f32_e32 v66, v60, v58
	v_and_b32_e32 v58, 0xffff0000, v57
	v_fmac_f32_e32 v66, v61, v58
	v_add_f32_e32 v68, v64, v66
	ds_read_b128 v[64:67], v173 offset:256
	v_mov_b32_e32 v58, v240
	v_mov_b32_e32 v59, v241
	v_mov_b32_e32 v60, v242
	v_mov_b32_e32 v61, v243
	v_and_b32_e32 v70, 0xffff0000, v58
	v_lshlrev_b32_e32 v69, 16, v58
	s_waitcnt lgkmcnt(0)
	v_mul_f32_e32 v70, v65, v70
	v_fmac_f32_e32 v70, v64, v69
	v_lshlrev_b32_e32 v64, 16, v59
	v_fmac_f32_e32 v70, v66, v64
	v_and_b32_e32 v64, 0xffff0000, v59
	v_fmac_f32_e32 v70, v67, v64
	ds_read_b128 v[64:67], v173 offset:272
	v_lshlrev_b32_e32 v69, 16, v60
	s_waitcnt lgkmcnt(0)
	v_fmac_f32_e32 v70, v64, v69
	v_and_b32_e32 v64, 0xffff0000, v60
	v_fmac_f32_e32 v70, v65, v64
	v_lshlrev_b32_e32 v64, 16, v61
	v_fmac_f32_e32 v70, v66, v64
	v_and_b32_e32 v64, 0xffff0000, v61
	v_fmac_f32_e32 v70, v67, v64
	v_add_f32_e32 v66, v68, v70
	ds_read_b128 v[62:65], v173 offset:384
	v_mov_b32_e32 v70, v248
	v_mov_b32_e32 v71, v249
	v_mov_b32_e32 v72, v250
	v_mov_b32_e32 v73, v251
	v_and_b32_e32 v68, 0xffff0000, v70
	v_lshlrev_b32_e32 v67, 16, v70
	s_waitcnt lgkmcnt(0)
	v_mul_f32_e32 v68, v63, v68
	v_fmac_f32_e32 v68, v62, v67
	v_lshlrev_b32_e32 v62, 16, v71
	v_fmac_f32_e32 v68, v64, v62
	v_and_b32_e32 v62, 0xffff0000, v71
	v_fmac_f32_e32 v68, v65, v62
	ds_read_b128 v[62:65], v173 offset:400
	v_lshlrev_b32_e32 v67, 16, v72
	s_waitcnt lgkmcnt(0)
	v_fmac_f32_e32 v68, v62, v67
	v_and_b32_e32 v62, 0xffff0000, v72
	v_fmac_f32_e32 v68, v63, v62
	v_lshlrev_b32_e32 v62, 16, v73
	v_fmac_f32_e32 v68, v64, v62
	v_and_b32_e32 v62, 0xffff0000, v73
	v_fmac_f32_e32 v68, v65, v62
	v_add_f32_e32 v62, v66, v68
	ds_bpermute_b32 v63, v175, v62
	ds_read_b128 v[66:69], v213 offset:64
	s_waitcnt lgkmcnt(1)
	v_add_f32_e32 v203, v62, v63
	ds_read_b128 v[62:65], v213
	s_waitcnt lgkmcnt(0)
	v_mfma_f32_16x16x32_bf16 v[62:65], v[62:65], v[50:53], 0
	ds_bpermute_b32 v209, v177, v203
	v_mfma_f32_16x16x32_bf16 v[62:65], v[66:69], v[54:57], v[62:65]
	ds_read_b128 v[66:69], v213 offset:128
	s_waitcnt lgkmcnt(0)
	v_mfma_f32_16x16x32_bf16 v[62:65], v[66:69], v[58:61], v[62:65]
	ds_read_b128 v[66:69], v213 offset:192
	s_waitcnt lgkmcnt(0)
	v_mfma_f32_16x16x32_bf16 v[62:65], v[66:69], v[70:73], v[62:65]
	ds_read_b128 v[66:69], v213 offset:4352
	s_waitcnt lgkmcnt(0)
	v_mfma_f32_16x16x32_bf16 v[66:69], v[66:69], v[50:53], 0
	v_mfma_f32_16x16x32_bf16 v[66:69], v[74:77], v[54:57], v[66:69]
	ds_read_b128 v[74:77], v213 offset:4480
	s_waitcnt lgkmcnt(0)
	v_mfma_f32_16x16x32_bf16 v[66:69], v[74:77], v[58:61], v[66:69]
	ds_read_b128 v[74:77], v213 offset:4544
	s_waitcnt lgkmcnt(0)
	v_mfma_f32_16x16x32_bf16 v[66:69], v[74:77], v[70:73], v[66:69]
	ds_read_b128 v[74:77], v213 offset:8704
	s_waitcnt lgkmcnt(0)
	v_mfma_f32_16x16x32_bf16 v[74:77], v[74:77], v[50:53], 0
	v_mfma_f32_16x16x32_bf16 v[74:77], v[78:81], v[54:57], v[74:77]
	ds_read_b128 v[78:81], v213 offset:8832
	s_waitcnt lgkmcnt(0)
	v_mfma_f32_16x16x32_bf16 v[74:77], v[78:81], v[58:61], v[74:77]
	ds_read_b128 v[78:81], v213 offset:8896
	s_waitcnt lgkmcnt(0)
	v_mfma_f32_16x16x32_bf16 v[74:77], v[78:81], v[70:73], v[74:77]
	ds_read_b128 v[78:81], v213 offset:13056
	s_waitcnt lgkmcnt(0)
	v_mfma_f32_16x16x32_bf16 v[78:81], v[78:81], v[50:53], 0
	v_mfma_f32_16x16x32_bf16 v[78:81], v[82:85], v[54:57], v[78:81]
	ds_read_b128 v[82:85], v213 offset:13184
	s_waitcnt lgkmcnt(0)
	v_mfma_f32_16x16x32_bf16 v[78:81], v[82:85], v[58:61], v[78:81]
	ds_read_b128 v[82:85], v213 offset:13248
	ds_read_b128 v[86:89], v213 offset:17472
	s_waitcnt lgkmcnt(1)
	v_mfma_f32_16x16x32_bf16 v[78:81], v[82:85], v[70:73], v[78:81]
	ds_read_b128 v[82:85], v213 offset:17408
	ds_read_b128 v[90:93], v213 offset:21824
	ds_read_b128 v[94:97], v213 offset:26176
	s_waitcnt lgkmcnt(2)
	v_mfma_f32_16x16x32_bf16 v[82:85], v[82:85], v[50:53], 0
	ds_read_b128 v[98:101], v213 offset:30528
	v_mfma_f32_16x16x32_bf16 v[82:85], v[86:89], v[54:57], v[82:85]
	ds_read_b128 v[86:89], v213 offset:17536
	s_waitcnt lgkmcnt(0)
	v_mfma_f32_16x16x32_bf16 v[82:85], v[86:89], v[58:61], v[82:85]
	ds_read_b128 v[86:89], v213 offset:17600
	s_waitcnt lgkmcnt(0)
	v_mfma_f32_16x16x32_bf16 v[82:85], v[86:89], v[70:73], v[82:85]
	ds_read_b128 v[86:89], v213 offset:21760
	s_waitcnt lgkmcnt(0)
	v_mfma_f32_16x16x32_bf16 v[86:89], v[86:89], v[50:53], 0
	v_mfma_f32_16x16x32_bf16 v[86:89], v[90:93], v[54:57], v[86:89]
	ds_read_b128 v[90:93], v213 offset:21888
	s_waitcnt lgkmcnt(0)
	v_mfma_f32_16x16x32_bf16 v[86:89], v[90:93], v[58:61], v[86:89]
	ds_read_b128 v[90:93], v213 offset:21952
	s_waitcnt lgkmcnt(0)
	v_mfma_f32_16x16x32_bf16 v[86:89], v[90:93], v[70:73], v[86:89]
	ds_read_b128 v[90:93], v213 offset:26112
	s_waitcnt lgkmcnt(0)
	v_mfma_f32_16x16x32_bf16 v[90:93], v[90:93], v[50:53], 0
	v_mfma_f32_16x16x32_bf16 v[90:93], v[94:97], v[54:57], v[90:93]
	ds_read_b128 v[94:97], v213 offset:26240
	s_waitcnt lgkmcnt(0)
	v_mfma_f32_16x16x32_bf16 v[90:93], v[94:97], v[58:61], v[90:93]
	ds_read_b128 v[94:97], v213 offset:26304
	s_waitcnt lgkmcnt(0)
	v_mfma_f32_16x16x32_bf16 v[90:93], v[94:97], v[70:73], v[90:93]
	ds_read_b128 v[94:97], v213 offset:30464
	s_waitcnt lgkmcnt(0)
	v_mfma_f32_16x16x32_bf16 v[94:97], v[94:97], v[50:53], 0
	v_mfma_f32_16x16x32_bf16 v[94:97], v[98:101], v[54:57], v[94:97]
	ds_read_b128 v[98:101], v213 offset:30592
	s_waitcnt lgkmcnt(0)
	v_mfma_f32_16x16x32_bf16 v[94:97], v[98:101], v[58:61], v[94:97]
	ds_read_b128 v[98:101], v213 offset:30656
	ds_read_b128 v[102:105], v213 offset:34880
	s_waitcnt lgkmcnt(1)
	v_mfma_f32_16x16x32_bf16 v[94:97], v[98:101], v[70:73], v[94:97]
	ds_read_b128 v[98:101], v213 offset:34816
	ds_read_b128 v[106:109], v213 offset:39232
	ds_read_b128 v[110:113], v213 offset:43584
	s_waitcnt lgkmcnt(2)
	v_mfma_f32_16x16x32_bf16 v[98:101], v[98:101], v[50:53], 0
	ds_read_b128 v[114:117], v213 offset:47936
	v_mfma_f32_16x16x32_bf16 v[98:101], v[102:105], v[54:57], v[98:101]
	ds_read_b128 v[102:105], v213 offset:34944
	s_waitcnt lgkmcnt(0)
	v_mfma_f32_16x16x32_bf16 v[98:101], v[102:105], v[58:61], v[98:101]
	ds_read_b128 v[102:105], v213 offset:35008
	s_waitcnt lgkmcnt(0)
	v_mfma_f32_16x16x32_bf16 v[98:101], v[102:105], v[70:73], v[98:101]
	ds_read_b128 v[102:105], v213 offset:39168
	s_waitcnt lgkmcnt(0)
	v_mfma_f32_16x16x32_bf16 v[102:105], v[102:105], v[50:53], 0
	v_mfma_f32_16x16x32_bf16 v[102:105], v[106:109], v[54:57], v[102:105]
	ds_read_b128 v[106:109], v213 offset:39296
	s_waitcnt lgkmcnt(0)
	v_mfma_f32_16x16x32_bf16 v[102:105], v[106:109], v[58:61], v[102:105]
	ds_read_b128 v[106:109], v213 offset:39360
	s_waitcnt lgkmcnt(0)
	v_mfma_f32_16x16x32_bf16 v[102:105], v[106:109], v[70:73], v[102:105]
	ds_read_b128 v[106:109], v213 offset:43520
	s_waitcnt lgkmcnt(0)
	v_mfma_f32_16x16x32_bf16 v[106:109], v[106:109], v[50:53], 0
	v_mfma_f32_16x16x32_bf16 v[106:109], v[110:113], v[54:57], v[106:109]
	ds_read_b128 v[110:113], v213 offset:43648
	s_waitcnt lgkmcnt(0)
	v_mfma_f32_16x16x32_bf16 v[106:109], v[110:113], v[58:61], v[106:109]
	ds_read_b128 v[110:113], v213 offset:43712
	s_waitcnt lgkmcnt(0)
	v_mfma_f32_16x16x32_bf16 v[106:109], v[110:113], v[70:73], v[106:109]
	ds_read_b128 v[110:113], v213 offset:47872
	s_waitcnt lgkmcnt(0)
	v_mfma_f32_16x16x32_bf16 v[110:113], v[110:113], v[50:53], 0
	v_mfma_f32_16x16x32_bf16 v[110:113], v[114:117], v[54:57], v[110:113]
	ds_read_b128 v[114:117], v213 offset:48000
	s_waitcnt lgkmcnt(0)
	v_mfma_f32_16x16x32_bf16 v[110:113], v[114:117], v[58:61], v[110:113]
	ds_read_b128 v[114:117], v213 offset:48064
	ds_read_b128 v[118:121], v213 offset:52288
	s_waitcnt lgkmcnt(1)
	v_mfma_f32_16x16x32_bf16 v[110:113], v[114:117], v[70:73], v[110:113]
	ds_read_b128 v[114:117], v213 offset:52224
	ds_read_b128 v[122:125], v213 offset:56640
	ds_read_b128 v[126:129], v213 offset:60992
	s_waitcnt lgkmcnt(2)
	v_mfma_f32_16x16x32_bf16 v[114:117], v[114:117], v[50:53], 0
	ds_read_b128 v[132:135], v213 offset:65344
	v_mfma_f32_16x16x32_bf16 v[114:117], v[118:121], v[54:57], v[114:117]
	ds_read_b128 v[118:121], v213 offset:52352
	s_waitcnt lgkmcnt(0)
	v_mfma_f32_16x16x32_bf16 v[114:117], v[118:121], v[58:61], v[114:117]
	ds_read_b128 v[118:121], v213 offset:52416
	s_waitcnt lgkmcnt(0)
	v_mfma_f32_16x16x32_bf16 v[114:117], v[118:121], v[70:73], v[114:117]
	ds_read_b128 v[118:121], v213 offset:56576
	s_waitcnt lgkmcnt(0)
	v_mfma_f32_16x16x32_bf16 v[118:121], v[118:121], v[50:53], 0
	v_mfma_f32_16x16x32_bf16 v[118:121], v[122:125], v[54:57], v[118:121]
	ds_read_b128 v[122:125], v213 offset:56704
	s_waitcnt lgkmcnt(0)
	v_mfma_f32_16x16x32_bf16 v[118:121], v[122:125], v[58:61], v[118:121]
	ds_read_b128 v[122:125], v213 offset:56768
	s_waitcnt lgkmcnt(0)
	v_mfma_f32_16x16x32_bf16 v[118:121], v[122:125], v[70:73], v[118:121]
	ds_read_b128 v[122:125], v213 offset:60928
	s_waitcnt lgkmcnt(0)
	v_mfma_f32_16x16x32_bf16 v[122:125], v[122:125], v[50:53], 0
	v_mfma_f32_16x16x32_bf16 v[122:125], v[126:129], v[54:57], v[122:125]
	ds_read_b128 v[126:129], v213 offset:61056
	s_waitcnt lgkmcnt(0)
	v_mfma_f32_16x16x32_bf16 v[122:125], v[126:129], v[58:61], v[122:125]
	ds_read_b128 v[126:129], v213 offset:61120
	s_waitcnt lgkmcnt(0)
	v_mfma_f32_16x16x32_bf16 v[122:125], v[126:129], v[70:73], v[122:125]
	ds_read_b128 v[126:129], v213 offset:65280
	s_waitcnt lgkmcnt(0)
	v_mfma_f32_16x16x32_bf16 v[126:129], v[126:129], v[50:53], 0
	v_mfma_f32_16x16x32_bf16 v[126:129], v[132:135], v[54:57], v[126:129]
	ds_read_b128 v[132:135], v213 offset:65408
	s_waitcnt lgkmcnt(0)
	v_mfma_f32_16x16x32_bf16 v[126:129], v[132:135], v[58:61], v[126:129]
	ds_read_b128 v[132:135], v213 offset:65472
	s_waitcnt lgkmcnt(0)
	v_mfma_f32_16x16x32_bf16 v[126:129], v[132:135], v[70:73], v[126:129]
	v_mad_u64_u32 v[132:133], s[70:71], v131, s3, v[138:139]
	v_mad_i32_i24 v133, s31, v216, v133
	global_load_dwordx4 v[142:145], v[132:133], off
	global_load_dwordx4 v[146:149], v[132:133], off offset:64
	global_load_dwordx4 v[150:153], v[132:133], off offset:128
	global_load_dwordx4 v[154:157], v[132:133], off offset:192
	v_cndmask_b32_e64 v131, 0, 1, s[94:95]
	v_cmp_ne_u32_e64 s[74:75], 1, v131
	s_mulk_i32 s31, 0x600
	s_cbranch_vccz .LBB0_665
	v_cndmask_b32_e64 v131, 0, 1, s[86:87]
	v_cmp_ne_u32_e64 s[70:71], 1, v131
	s_andn2_b64 vcc, exec, s[86:87]
	s_cbranch_vccz .LBB0_666
